# pool2: compare-and-swap accumulation starts speculatively from +0.0 (one LDS round trip for first contributions) instead of read-then-CAS
# speedup vs baseline: 1.0261x; 1.0038x over previous
.LBB4_23:
	v_min_i32_e32 v71, v105, v101
	v_add_u32_e32 v109, 0x200, v105
	v_min_i32_e32 v74, v109, v101
	v_add_u32_e32 v108, 0x400, v105
	s_waitcnt lgkmcnt(0)
	v_cmp_gt_i32_e32 vcc, v102, v71
	s_waitcnt vmcnt(0)
	v_min_i32_e32 v75, v108, v101
	v_add_u32_e32 v107, 0x600, v105
	v_cndmask_b32_e64 v72, 64, 0, vcc
	v_cmp_gt_i32_e32 vcc, v102, v74
	v_min_i32_e32 v76, v107, v101
	v_add_u32_e32 v106, 0x800, v105
	v_cndmask_b32_e64 v73, 64, 0, vcc
	v_cmp_gt_i32_e32 vcc, v102, v75
	v_min_i32_e32 v70, v106, v101
	v_lshl_add_u32 v81, v72, 2, v98
	v_cndmask_b32_e64 v77, 64, 0, vcc
	v_cmp_gt_i32_e32 vcc, v102, v76
	v_lshl_add_u32 v83, v73, 2, v98
	v_lshl_add_u32 v85, v77, 2, v98
	v_cndmask_b32_e64 v78, 64, 0, vcc
	v_cmp_gt_i32_e32 vcc, v102, v70
	v_lshl_add_u32 v88, v78, 2, v98
	v_or_b32_e32 v80, 32, v72
	v_cndmask_b32_e64 v79, 64, 0, vcc
	v_lshl_add_u32 v110, v79, 2, v98
	ds_read_b32 v81, v81 offset:128
	ds_read_b32 v83, v83 offset:128
	ds_read_b32 v85, v85 offset:128
	ds_read_b32 v88, v88 offset:128
	ds_read_b32 v110, v110 offset:128
	s_waitcnt lgkmcnt(4)
	v_cmp_gt_i32_e32 vcc, v81, v71
	v_or_b32_e32 v82, 32, v73
	v_or_b32_e32 v84, 32, v77
	v_cndmask_b32_e32 v72, v80, v72, vcc
	s_waitcnt lgkmcnt(3)
	v_cmp_gt_i32_e32 vcc, v83, v74
	v_or_b32_e32 v86, 32, v78
	v_or_b32_e32 v89, 32, v79
	v_cndmask_b32_e32 v73, v82, v73, vcc
	s_waitcnt lgkmcnt(2)
	v_cmp_gt_i32_e32 vcc, v85, v75
	v_lshl_add_u32 v81, v72, 2, v98
	v_lshl_add_u32 v83, v73, 2, v98
	v_cndmask_b32_e32 v77, v84, v77, vcc
	s_waitcnt lgkmcnt(1)
	v_cmp_gt_i32_e32 vcc, v88, v76
	v_lshl_add_u32 v85, v77, 2, v98
	v_or_b32_e32 v80, 16, v72
	v_cndmask_b32_e32 v78, v86, v78, vcc
	s_waitcnt lgkmcnt(0)
	v_cmp_gt_i32_e32 vcc, v110, v70
	v_lshl_add_u32 v88, v78, 2, v98
	v_or_b32_e32 v82, 16, v73
	v_cndmask_b32_e32 v79, v89, v79, vcc
	v_lshl_add_u32 v110, v79, 2, v98
	ds_read_b32 v81, v81 offset:64
	ds_read_b32 v83, v83 offset:64
	ds_read_b32 v85, v85 offset:64
	ds_read_b32 v88, v88 offset:64
	ds_read_b32 v110, v110 offset:64
	s_waitcnt lgkmcnt(4)
	v_cmp_gt_i32_e32 vcc, v81, v71
	v_or_b32_e32 v84, 16, v77
	v_or_b32_e32 v86, 16, v78
	v_cndmask_b32_e32 v72, v80, v72, vcc
	s_waitcnt lgkmcnt(3)
	v_cmp_gt_i32_e32 vcc, v83, v74
	v_or_b32_e32 v89, 16, v79
	v_lshl_add_u32 v81, v72, 2, v98
	v_cndmask_b32_e32 v73, v82, v73, vcc
	s_waitcnt lgkmcnt(2)
	v_cmp_gt_i32_e32 vcc, v85, v75
	v_lshl_add_u32 v83, v73, 2, v98
	v_or_b32_e32 v80, 8, v72
	v_cndmask_b32_e32 v77, v84, v77, vcc
	s_waitcnt lgkmcnt(1)
	v_cmp_gt_i32_e32 vcc, v88, v76
	v_lshl_add_u32 v85, v77, 2, v98
	v_or_b32_e32 v82, 8, v73
	v_cndmask_b32_e32 v78, v86, v78, vcc
	s_waitcnt lgkmcnt(0)
	v_cmp_gt_i32_e32 vcc, v110, v70
	v_lshl_add_u32 v88, v78, 2, v98
	v_or_b32_e32 v84, 8, v77
	v_cndmask_b32_e32 v79, v89, v79, vcc
	v_lshl_add_u32 v110, v79, 2, v98
	ds_read_b32 v81, v81 offset:32
	ds_read_b32 v83, v83 offset:32
	ds_read_b32 v85, v85 offset:32
	ds_read_b32 v88, v88 offset:32
	ds_read_b32 v110, v110 offset:32
	s_waitcnt lgkmcnt(4)
	v_cmp_gt_i32_e32 vcc, v81, v71
	v_or_b32_e32 v86, 8, v78
	v_or_b32_e32 v89, 8, v79
	v_cndmask_b32_e32 v72, v80, v72, vcc
	s_waitcnt lgkmcnt(3)
	v_cmp_gt_i32_e32 vcc, v83, v74
	v_lshl_add_u32 v81, v72, 2, v98
	v_add_u32_e32 v80, 4, v72
	v_cndmask_b32_e32 v73, v82, v73, vcc
	s_waitcnt lgkmcnt(2)
	v_cmp_gt_i32_e32 vcc, v85, v75
	v_lshl_add_u32 v83, v73, 2, v98
	v_add_u32_e32 v82, 4, v73
	v_cndmask_b32_e32 v77, v84, v77, vcc
	s_waitcnt lgkmcnt(1)
	v_cmp_gt_i32_e32 vcc, v88, v76
	v_lshl_add_u32 v85, v77, 2, v98
	v_add_u32_e32 v84, 4, v77
	v_cndmask_b32_e32 v78, v86, v78, vcc
	s_waitcnt lgkmcnt(0)
	v_cmp_gt_i32_e32 vcc, v110, v70
	v_lshl_add_u32 v88, v78, 2, v98
	v_add_u32_e32 v86, 4, v78
	v_cndmask_b32_e32 v79, v89, v79, vcc
	v_lshl_add_u32 v110, v79, 2, v98
	ds_read_b32 v81, v81 offset:16
	ds_read_b32 v83, v83 offset:16
	ds_read_b32 v85, v85 offset:16
	ds_read_b32 v88, v88 offset:16
	ds_read_b32 v110, v110 offset:16
	s_waitcnt lgkmcnt(4)
	v_cmp_gt_i32_e32 vcc, v81, v71
	v_add_u32_e32 v89, 4, v79
	s_nop 0
	v_cndmask_b32_e32 v72, v80, v72, vcc
	s_waitcnt lgkmcnt(3)
	v_cmp_gt_i32_e32 vcc, v83, v74
	v_lshl_add_u32 v81, v72, 2, v98
	v_add_u32_e32 v80, 2, v72
	v_cndmask_b32_e32 v73, v82, v73, vcc
	s_waitcnt lgkmcnt(2)
	v_cmp_gt_i32_e32 vcc, v85, v75
	v_lshl_add_u32 v83, v73, 2, v98
	v_add_u32_e32 v82, 2, v73
	v_cndmask_b32_e32 v77, v84, v77, vcc
	s_waitcnt lgkmcnt(1)
	v_cmp_gt_i32_e32 vcc, v88, v76
	v_lshl_add_u32 v85, v77, 2, v98
	v_add_u32_e32 v84, 2, v77
	v_cndmask_b32_e32 v78, v86, v78, vcc
	s_waitcnt lgkmcnt(0)
	v_cmp_gt_i32_e32 vcc, v110, v70
	v_lshl_add_u32 v88, v78, 2, v98
	v_add_u32_e32 v86, 2, v78
	v_cndmask_b32_e32 v79, v89, v79, vcc
	v_lshl_add_u32 v110, v79, 2, v98
	ds_read_b32 v81, v81 offset:8
	ds_read_b32 v83, v83 offset:8
	ds_read_b32 v85, v85 offset:8
	ds_read_b32 v88, v88 offset:8
	ds_read_b32 v110, v110 offset:8
	s_waitcnt lgkmcnt(4)
	v_cmp_gt_i32_e32 vcc, v81, v71
	v_add_u32_e32 v89, 2, v79
	s_nop 0
	v_cndmask_b32_e32 v72, v80, v72, vcc
	s_waitcnt lgkmcnt(3)
	v_cmp_gt_i32_e32 vcc, v83, v74
	v_lshl_add_u32 v81, v72, 2, v98
	v_add_u32_e32 v80, 1, v72
	v_cndmask_b32_e32 v73, v82, v73, vcc
	s_waitcnt lgkmcnt(2)
	v_cmp_gt_i32_e32 vcc, v85, v75
	v_lshl_add_u32 v83, v73, 2, v98
	v_add_u32_e32 v82, 1, v73
	v_cndmask_b32_e32 v77, v84, v77, vcc
	s_waitcnt lgkmcnt(1)
	v_cmp_gt_i32_e32 vcc, v88, v76
	v_lshl_add_u32 v85, v77, 2, v98
	v_add_u32_e32 v84, 1, v77
	v_cndmask_b32_e32 v78, v86, v78, vcc
	s_waitcnt lgkmcnt(0)
	v_cmp_gt_i32_e32 vcc, v110, v70
	v_lshl_add_u32 v88, v78, 2, v98
	v_add_u32_e32 v86, 1, v78
	v_cndmask_b32_e32 v79, v89, v79, vcc
	v_lshl_add_u32 v110, v79, 2, v98
	ds_read_b32 v81, v81 offset:4
	ds_read_b32 v83, v83 offset:4
	ds_read_b32 v85, v85 offset:4
	ds_read_b32 v88, v88 offset:4
	ds_read_b32 v110, v110 offset:4
	s_waitcnt lgkmcnt(4)
	v_cmp_gt_i32_e32 vcc, v81, v71
	v_add_u32_e32 v89, 1, v79
	s_nop 0
	v_cndmask_b32_e32 v72, v80, v72, vcc
	s_waitcnt lgkmcnt(3)
	v_cmp_gt_i32_e32 vcc, v83, v74
	v_lshlrev_b32_e32 v72, 2, v72
	v_add_u32_e32 v80, v97, v72
	v_cndmask_b32_e32 v73, v82, v73, vcc
	s_waitcnt lgkmcnt(2)
	v_cmp_gt_i32_e32 vcc, v85, v75
	v_lshlrev_b32_e32 v73, 2, v73
	v_add_u32_e32 v72, v98, v72
	v_cndmask_b32_e32 v77, v84, v77, vcc
	s_waitcnt lgkmcnt(1)
	v_cmp_gt_i32_e32 vcc, v88, v76
	v_lshlrev_b32_e32 v77, 2, v77
	v_add_u32_e32 v81, v97, v73
	v_cndmask_b32_e32 v78, v86, v78, vcc
	v_lshlrev_b32_e32 v78, 2, v78
	v_add_u32_e32 v82, v97, v77
	v_add_u32_e32 v77, v98, v77
	v_add_u32_e32 v83, v97, v78
	v_add_u32_e32 v78, v98, v78
	v_add_u32_e32 v73, v98, v73
	ds_read_b32 v80, v80
	ds_read_b32 v72, v72
	ds_read_b32 v81, v81
	ds_read_b32 v84, v73
	ds_read_b32 v82, v82
	ds_read_b32 v77, v77
	ds_read_b32 v83, v83
	ds_read_b32 v78, v78
	s_waitcnt lgkmcnt(7)
	v_add_u32_e32 v71, v80, v71
	s_waitcnt lgkmcnt(6)
	v_sub_u32_e32 v72, v71, v72
	v_ashrrev_i32_e32 v73, 31, v72
	v_lshl_add_u64 v[72:73], v[72:73], 2, s[16:17]
	s_waitcnt lgkmcnt(5)
	v_add_u32_e32 v71, v81, v74
	global_load_dword v116, v[72:73], off
	s_waitcnt lgkmcnt(4)
	v_sub_u32_e32 v72, v71, v84
	v_ashrrev_i32_e32 v73, 31, v72
	v_lshl_add_u64 v[72:73], v[72:73], 2, s[16:17]
	s_waitcnt lgkmcnt(3)
	v_add_u32_e32 v71, v82, v75
	global_load_dword v114, v[72:73], off
	s_waitcnt lgkmcnt(2)
	v_sub_u32_e32 v72, v71, v77
	v_cmp_gt_i32_e32 vcc, v110, v70
	v_ashrrev_i32_e32 v73, 31, v72
	v_lshl_add_u64 v[72:73], v[72:73], 2, s[16:17]
	v_cndmask_b32_e32 v79, v89, v79, vcc
	s_waitcnt lgkmcnt(1)
	v_add_u32_e32 v71, v83, v76
	global_load_dword v112, v[72:73], off
	s_waitcnt lgkmcnt(0)
	v_sub_u32_e32 v72, v71, v78
	v_lshlrev_b32_e32 v71, 2, v79
	v_add_u32_e32 v73, v97, v71
	v_add_u32_e32 v71, v98, v71
	ds_read_b32 v74, v73
	ds_read_b32 v71, v71
	v_ashrrev_i32_e32 v73, 31, v72
	v_lshl_add_u64 v[72:73], v[72:73], 2, s[16:17]
	global_load_dword v111, v[72:73], off
	s_waitcnt lgkmcnt(1)
	v_add_u32_e32 v70, v74, v70
	s_waitcnt lgkmcnt(0)
	v_sub_u32_e32 v70, v70, v71
	v_ashrrev_i32_e32 v71, 31, v70
	v_lshl_add_u64 v[70:71], v[70:71], 2, s[16:17]
	global_load_dword v110, v[70:71], off
	s_waitcnt vmcnt(4)
	v_lshlrev_b32_sdwa v88, v103, v116 dst_sel:DWORD dst_unused:UNUSED_PAD src0_sel:DWORD src1_sel:WORD_0
	v_add_u32_sdwa v86, v116, v95 dst_sel:DWORD dst_unused:UNUSED_PAD src0_sel:WORD_1 src1_sel:DWORD
	v_lshl_add_u32 v86, v86, 2, v123
	ds_read_b32 v119, v86
	global_load_dwordx4 v[124:127], v88, s[10:11]
	s_waitcnt vmcnt(4)
	v_lshlrev_b32_sdwa v70, v103, v114 dst_sel:DWORD dst_unused:UNUSED_PAD src0_sel:DWORD src1_sel:WORD_0
	v_add_u32_sdwa v86, v114, v95 dst_sel:DWORD dst_unused:UNUSED_PAD src0_sel:WORD_1 src1_sel:DWORD
	global_load_dwordx4 v[82:85], v70, s[10:11]
	v_lshl_add_u32 v86, v86, 2, v123
	ds_read_b32 v118, v86
	s_waitcnt vmcnt(4)
	v_lshlrev_b32_sdwa v70, v103, v112 dst_sel:DWORD dst_unused:UNUSED_PAD src0_sel:DWORD src1_sel:WORD_0
	v_add_u32_sdwa v86, v112, v95 dst_sel:DWORD dst_unused:UNUSED_PAD src0_sel:WORD_1 src1_sel:DWORD
	global_load_dwordx4 v[78:81], v70, s[10:11]
	v_lshl_add_u32 v86, v86, 2, v123
	ds_read_b32 v117, v86
	s_waitcnt vmcnt(4)
	v_lshlrev_b32_sdwa v70, v103, v111 dst_sel:DWORD dst_unused:UNUSED_PAD src0_sel:DWORD src1_sel:WORD_0
	v_add_u32_sdwa v86, v111, v95 dst_sel:DWORD dst_unused:UNUSED_PAD src0_sel:WORD_1 src1_sel:DWORD
	global_load_dwordx4 v[74:77], v70, s[10:11]
	v_lshl_add_u32 v86, v86, 2, v123
	ds_read_b32 v115, v86
	s_waitcnt vmcnt(4)
	v_add_u32_sdwa v86, v110, v95 dst_sel:DWORD dst_unused:UNUSED_PAD src0_sel:WORD_1 src1_sel:DWORD
	v_lshl_add_u32 v86, v86, 2, v123
	ds_read_b32 v113, v86
	v_lshlrev_b32_sdwa v70, v103, v110 dst_sel:DWORD dst_unused:UNUSED_PAD src0_sel:DWORD src1_sel:WORD_0
	global_load_dwordx4 v[70:73], v70, s[10:11]
	s_waitcnt vmcnt(4) lgkmcnt(4)
	v_cmp_gt_u32_e32 vcc, 64, v127
	s_and_saveexec_b64 s[0:1], vcc
	s_cbranch_execz .LBB4_25
	v_lshlrev_b32_sdwa v89, v104, v116 dst_sel:DWORD dst_unused:UNUSED_PAD src0_sel:DWORD src1_sel:WORD_1
	v_add_f32_e32 v86, v119, v124
	v_mul_f32_e32 v88, 0x3e4ccccd, v86
	v_max_f32_e32 v86, v86, v88
	v_sub_f32_e32 v86, v86, v125
	v_exp_f32_e32 v86, v86
	v_mul_lo_u32 v88, v127, s3
	v_add3_u32 v88, v99, v88, v89
	v_mul_f32_e32 v86, v126, v86
	v_mov_b32_e32 v124, 0
.Lp2_cas_s0:
	v_add_f32_e32 v125, v124, v86
	ds_cmpst_rtn_b32 v89, v88, v124, v125
	s_waitcnt lgkmcnt(0)
	v_cmp_ne_u32_e32 vcc, v89, v124
	v_mov_b32_e32 v124, v89
	s_and_b64 exec, exec, vcc
	s_cbranch_execnz .Lp2_cas_s0
.LBB4_25:
	s_or_b64 exec, exec, s[0:1]
	v_cmp_lt_i32_e32 vcc, v109, v100
	s_waitcnt vmcnt(3)
	v_cmp_gt_u32_e64 s[0:1], 64, v85
	s_and_b64 s[18:19], vcc, s[0:1]
	s_and_saveexec_b64 s[0:1], s[18:19]
	s_cbranch_execz .LBB4_27
	s_waitcnt lgkmcnt(3)
	v_add_f32_e32 v82, v118, v82
	v_mul_f32_e32 v86, 0x3e4ccccd, v82
	v_max_f32_e32 v82, v82, v86
	v_sub_f32_e32 v82, v82, v83
	v_exp_f32_e32 v82, v82
	v_mul_lo_u32 v83, v85, s3
	v_lshlrev_b32_sdwa v85, v104, v114 dst_sel:DWORD dst_unused:UNUSED_PAD src0_sel:DWORD src1_sel:WORD_1
	v_add3_u32 v83, v99, v83, v85
	v_mul_f32_e32 v82, v84, v82
	v_mov_b32_e32 v84, 0
.Lp2_cas_s1:
	v_add_f32_e32 v85, v84, v82
	ds_cmpst_rtn_b32 v86, v83, v84, v85
	s_waitcnt lgkmcnt(0)
	v_cmp_ne_u32_e32 vcc, v86, v84
	v_mov_b32_e32 v84, v86
	s_and_b64 exec, exec, vcc
	s_cbranch_execnz .Lp2_cas_s1
.LBB4_27:
	s_or_b64 exec, exec, s[0:1]
	v_cmp_lt_i32_e32 vcc, v108, v100
	s_waitcnt vmcnt(2)
	v_cmp_gt_u32_e64 s[0:1], 64, v81
	s_and_b64 s[18:19], vcc, s[0:1]
	s_and_saveexec_b64 s[0:1], s[18:19]
	s_cbranch_execz .LBB4_29
	s_waitcnt lgkmcnt(2)
	v_add_f32_e32 v78, v117, v78
	v_mul_f32_e32 v82, 0x3e4ccccd, v78
	v_max_f32_e32 v78, v78, v82
	v_sub_f32_e32 v78, v78, v79
	v_exp_f32_e32 v78, v78
	v_mul_lo_u32 v79, v81, s3
	v_lshlrev_b32_sdwa v81, v104, v112 dst_sel:DWORD dst_unused:UNUSED_PAD src0_sel:DWORD src1_sel:WORD_1
	v_add3_u32 v79, v99, v79, v81
	v_mul_f32_e32 v78, v80, v78
	v_mov_b32_e32 v80, 0
.Lp2_cas_s2:
	v_add_f32_e32 v81, v80, v78
	ds_cmpst_rtn_b32 v86, v79, v80, v81
	s_waitcnt lgkmcnt(0)
	v_cmp_ne_u32_e32 vcc, v86, v80
	v_mov_b32_e32 v80, v86
	s_and_b64 exec, exec, vcc
	s_cbranch_execnz .Lp2_cas_s2
.LBB4_29:
	s_or_b64 exec, exec, s[0:1]
	v_cmp_lt_i32_e32 vcc, v107, v100
	s_waitcnt vmcnt(1)
	v_cmp_gt_u32_e64 s[0:1], 64, v77
	s_and_b64 s[18:19], vcc, s[0:1]
	s_and_saveexec_b64 s[0:1], s[18:19]
	s_cbranch_execz .LBB4_31
	s_waitcnt lgkmcnt(1)
	v_add_f32_e32 v74, v115, v74
	v_mul_f32_e32 v78, 0x3e4ccccd, v74
	v_max_f32_e32 v74, v74, v78
	v_sub_f32_e32 v74, v74, v75
	v_exp_f32_e32 v74, v74
	v_mul_lo_u32 v75, v77, s3
	v_lshlrev_b32_sdwa v77, v104, v111 dst_sel:DWORD dst_unused:UNUSED_PAD src0_sel:DWORD src1_sel:WORD_1
	v_add3_u32 v75, v99, v75, v77
	v_mul_f32_e32 v74, v76, v74
	v_mov_b32_e32 v76, 0
.Lp2_cas_s3:
	v_add_f32_e32 v77, v76, v74
	ds_cmpst_rtn_b32 v86, v75, v76, v77
	s_waitcnt lgkmcnt(0)
	v_cmp_ne_u32_e32 vcc, v86, v76
	v_mov_b32_e32 v76, v86
	s_and_b64 exec, exec, vcc
	s_cbranch_execnz .Lp2_cas_s3
.LBB4_31:
	s_or_b64 exec, exec, s[0:1]
	v_cmp_lt_i32_e32 vcc, v106, v100
	s_waitcnt vmcnt(0) lgkmcnt(0)
	v_cmp_gt_u32_e64 s[0:1], 64, v73
	s_and_b64 s[18:19], vcc, s[0:1]
	s_and_saveexec_b64 s[0:1], s[18:19]
	s_cbranch_execz .LBB4_22
	v_add_f32_e32 v70, v113, v70
	v_mul_f32_e32 v74, 0x3e4ccccd, v70
	v_max_f32_e32 v70, v70, v74
	v_sub_f32_e32 v70, v70, v71
	v_exp_f32_e32 v70, v70
	v_mul_lo_u32 v71, v73, s3
	v_lshlrev_b32_sdwa v73, v104, v110 dst_sel:DWORD dst_unused:UNUSED_PAD src0_sel:DWORD src1_sel:WORD_1
	v_add3_u32 v71, v99, v71, v73
	v_mul_f32_e32 v70, v72, v70
	v_mov_b32_e32 v72, 0
.Lp2_cas_s4:
	v_add_f32_e32 v73, v72, v70
	ds_cmpst_rtn_b32 v86, v71, v72, v73
	s_waitcnt lgkmcnt(0)
	v_cmp_ne_u32_e32 vcc, v86, v72
	v_mov_b32_e32 v72, v86
	s_and_b64 exec, exec, vcc
	s_cbranch_execnz .Lp2_cas_s4
	s_branch .LBB4_22
.LBB4_33:
	s_or_b64 exec, exec, s[4:5]
	s_waitcnt vmcnt(1)
	v_cmp_gt_u32_e32 vcc, 64, v69
	s_and_b64 s[4:5], s[14:15], vcc
	s_and_saveexec_b64 s[0:1], s[4:5]
	s_cbranch_execz .LBB4_35
	s_waitcnt vmcnt(0)
	v_add_f32_e32 v66, v96, v66
	v_mul_f32_e32 v70, 0x3e4ccccd, v66
	v_max_f32_e32 v66, v66, v70
	v_sub_f32_e32 v66, v66, v67
	v_exp_f32_e32 v66, v66
	s_movk_i32 s3, 0x210
	v_mul_lo_u32 v67, v69, s3
	v_lshlrev_b32_e32 v69, 2, v94
	v_add3_u32 v67, v99, v67, v69
	v_mul_f32_e32 v66, v68, v66
	v_mov_b32_e32 v68, 0
.Lp2_cas_self:
	v_add_f32_e32 v69, v68, v66
	ds_cmpst_rtn_b32 v70, v67, v68, v69
	s_waitcnt lgkmcnt(0)
	v_cmp_ne_u32_e32 vcc, v70, v68
	v_mov_b32_e32 v68, v70
	s_and_b64 exec, exec, vcc
	s_cbranch_execnz .Lp2_cas_self
